# v44_touch2
# baseline (speedup 1.0000x reference)
_Z10k_enc_scanPKDF16_PKfS2_S2_S2_S2_S2_S2_S2_S2_S2_S0_S2_S2_S2_S2_S2_S0_S2_PfPjS2_S2_S2_S2_S2_S2_S2_S2_S2_S2_S2_S2_PDF16_S5_S3_:
	s_load_dwordx4 s[52:55], s[0:1], 0x98
	s_cmp_gt_u32 s2, 15
	s_mov_b64 s[4:5], -1
	s_cbranch_scc0 .LBB3_39
	s_add_i32 s3, s2, -16
	s_cmpk_gt_i32 s3, 0x33f
	s_cbranch_scc1 .LBB3_38
	v_add_u32_e32 v5, 0x140, v0
	v_add_u32_e32 v6, 0x280, v0
	v_mul_u32_u24_e32 v3, 0x5f5, v5
	v_add_u32_e32 v7, 0x3c0, v0
	v_lshrrev_b32_e32 v10, 17, v3
	v_mul_u32_u24_e32 v3, 0xbe9, v6
	v_add_u32_e32 v8, 0x500, v0
	v_lshrrev_b32_e32 v11, 18, v3
	v_mul_u32_u24_e32 v3, 0xbe9, v7
	v_add_u32_e32 v2, 0x640, v0
	v_lshrrev_b32_e32 v12, 18, v3
	v_mul_u32_u24_e32 v3, 0xbe9, v8
	s_load_dwordx2 s[20:21], s[0:1], 0x90
	s_load_dwordx4 s[56:59], s[0:1], 0x80
	s_load_dwordx8 s[12:19], s[0:1], 0x60
	s_load_dwordx8 s[24:31], s[0:1], 0x40
	s_load_dwordx8 s[36:43], s[0:1], 0x0
	s_load_dwordx8 s[44:51], s[0:1], 0x20
	v_lshrrev_b32_e32 v14, 18, v3
	v_mul_u32_u24_e32 v3, 0x17d1, v2
	s_movk_i32 s4, 0xffaa
	v_lshrrev_b32_e32 v16, 19, v3
	v_mad_i32_i24 v116, v16, s4, v2
	v_mul_u32_u24_e32 v2, 22, v0
	v_mov_b32_e32 v67, 0
	v_lshlrev_b32_e32 v66, 2, v2
	v_mul_u32_u24_e32 v2, 11, v0
	s_waitcnt lgkmcnt(0)
	v_lshl_add_u64 v[72:73], s[40:41], 0, v[66:67]
	v_lshlrev_b32_e32 v66, 2, v2
	v_lshrrev_b32_e32 v2, 1, v0
	v_lshl_add_u64 v[76:77], s[44:45], 0, v[66:67]
	v_and_b32_e32 v117, 0xfc, v2
	v_and_b32_e32 v2, 0x1c0, v0
	s_movk_i32 s8, 0xc0
	v_add_u32_e32 v66, 0xffffff40, v0
	v_cmp_eq_u32_e64 s[8:9], s8, v2
	v_lshlrev_b64 v[2:3], 2, v[66:67]
	v_lshl_add_u64 v[88:89], s[14:15], 0, v[2:3]
	v_lshl_add_u64 v[90:91], s[56:57], 0, v[2:3]
	v_lshl_add_u64 v[92:93], s[12:13], 0, v[2:3]
	v_lshl_add_u64 v[94:95], s[18:19], 0, v[2:3]
	v_lshl_add_u64 v[96:97], s[16:17], 0, v[2:3]
	v_mul_u32_u24_e32 v2, 0x5556, v0
	v_mov_b32_e32 v3, -3
	s_movk_i32 s18, 0x1a0
	v_mul_i32_i24_sdwa v3, v2, v3 dst_sel:DWORD dst_unused:UNUSED_PAD src0_sel:WORD_1 src1_sel:DWORD
	v_mul_u32_u24_sdwa v19, v2, s18 dst_sel:DWORD dst_unused:UNUSED_PAD src0_sel:WORD_1 src1_sel:DWORD
	v_mul_u32_u24_e32 v2, 0xa3e, v0
	v_lshrrev_b32_e32 v2, 12, v2
	v_mad_i32_i24 v112, v10, s4, v5
	v_mad_i32_i24 v113, v11, s4, v6
	v_mad_i32_i24 v114, v12, s4, v7
	v_mad_i32_i24 v115, v14, s4, v8
	v_add_lshl_u32 v20, v3, v0, 4
	v_mul_u32_u24_e32 v3, 0xa3e, v5
	v_mul_u32_u24_e32 v5, 0xa3e, v6
	v_mul_u32_u24_e32 v6, 0xa3e, v7
	v_mul_u32_u24_e32 v7, 0xa3e, v8
	v_and_b32_e32 v2, 0x1f0, v2
	v_lshlrev_b32_e32 v8, 4, v0
	v_add_u32_e32 v123, v2, v8
	v_lshrrev_b32_e32 v2, 12, v3
	v_and_b32_e32 v2, 0x3f0, v2
	v_add_u32_e32 v124, v2, v8
	v_lshrrev_b32_e32 v2, 12, v5
	v_and_b32_e32 v2, 0x7f0, v2
	v_add_u32_e32 v125, v2, v8
	v_lshrrev_b32_e32 v2, 12, v6
	v_and_b32_e32 v2, 0x7f0, v2
	v_mul_u32_u24_e32 v1, 0x2fb, v0
	v_add_u32_e32 v126, v2, v8
	v_lshrrev_b32_e32 v2, 12, v7
	v_and_b32_e32 v4, 63, v0
	v_lshrrev_b32_e32 v9, 16, v1
	v_and_b32_e32 v2, 0x7f0, v2
	v_mad_i32_i24 v1, v9, s4, v0
	v_and_b32_e32 v18, 15, v0
	v_add_u32_e32 v127, v2, v8
	v_lshrrev_b32_e32 v2, 2, v0
	s_movk_i32 s19, 0x70
	v_and_b32_e32 v98, 48, v0
	v_lshlrev_b32_e32 v66, 4, v4
	v_mov_b32_e32 v99, v67
	v_mov_b32_e32 v4, 0xfffff920
	v_and_or_b32 v128, v2, s19, v18
	v_lshl_add_u64 v[102:103], s[20:21], 0, v[98:99]
	v_mad_u64_u32 v[2:3], s[20:21], s2, 22, v[0:1]
	v_mov_b32_e32 v5, -1
	v_mad_u64_u32 v[104:105], s[20:21], v2, 5, v[4:5]
	v_min_u32_e32 v13, 21, v12
	v_min_u32_e32 v15, 21, v14
	v_min_u32_e32 v17, 21, v16
	s_movk_i32 s20, 0x410
	v_mov_b32_e32 v2, 0xfffa6a00
	v_mad_u32_u24 v99, v17, s20, v2
	v_mad_u32_u24 v105, v15, s20, v2
	v_mad_u32_u24 v130, v13, s20, v2
	v_mad_u32_u24 v131, v11, s20, v2
	v_mad_u32_u24 v132, v10, s20, v2
	v_mad_u32_u24 v133, v9, s20, v2
	v_lshlrev_b32_e32 v2, 6, v0
	s_mul_i32 s20, s2, 0x42000
	v_and_b32_e32 v2, 0x7000, v2
	v_add_u32_e32 v2, s20, v2
	v_lshlrev_b32_e32 v3, 8, v18
	v_lshlrev_b32_e32 v68, 2, v0
	v_mov_b32_e32 v69, v67
	s_movk_i32 s6, 0xb0
	s_movk_i32 s10, 0x102
	v_mul_lo_u32 v21, v1, s18
	v_lshlrev_b32_e32 v22, 4, v9
	v_mul_lo_u32 v23, v112, s18
	v_lshlrev_b32_e32 v24, 4, v10
	v_mul_lo_u32 v25, v113, s18
	v_lshlrev_b32_e32 v26, 4, v11
	s_movk_i32 s12, 0x3a4
	v_mul_lo_u32 v27, v114, s18
	v_lshlrev_b32_e32 v12, 4, v12
	s_movk_i32 s14, 0x264
	v_mul_lo_u32 v28, v115, s18
	v_lshlrev_b32_e32 v14, 4, v14
	s_movk_i32 s16, 0x124
	v_mul_lo_u32 v29, v116, s18
	v_lshlrev_b32_e32 v16, 4, v16
	v_mul_u32_u24_e32 v6, 0x1a0, v128
	v_or3_b32 v2, v2, v3, v98
	v_lshlrev_b32_e32 v106, 4, v0
	v_cmp_gt_u32_e64 s[22:23], 22, v0
	v_cmp_gt_u32_e64 s[4:5], 11, v0
	v_lshl_add_u64 v[70:71], s[42:43], 0, v[68:69]
	v_lshl_add_u64 v[74:75], s[46:47], 0, v[68:69]
	v_cmp_gt_u32_e64 s[6:7], s6, v0
	v_lshl_add_u64 v[78:79], s[50:51], 0, v[68:69]
	v_lshl_add_u64 v[80:81], s[28:29], 0, v[68:69]
	v_lshl_add_u64 v[82:83], s[48:49], 0, v[68:69]
	v_lshl_add_u64 v[84:85], s[26:27], 0, v[68:69]
	v_lshl_add_u64 v[86:87], s[24:25], 0, v[68:69]
	v_cmp_gt_u32_e64 s[10:11], s10, v0
	v_lshlrev_b32_e32 v69, 5, v9
	v_lshlrev_b32_e32 v118, 5, v10
	v_lshlrev_b32_e32 v119, 5, v11
	v_cmp_gt_u32_e64 s[12:13], s12, v0
	v_lshlrev_b32_e32 v120, 5, v13
	v_cmp_gt_u32_e64 s[14:15], s14, v0
	v_lshlrev_b32_e32 v121, 5, v15
	v_cmp_gt_u32_e64 s[16:17], s16, v0
	v_lshlrev_b32_e32 v122, 5, v17
	v_mad_u32_u24 v129, v18, s18, v98
	s_mov_b32 s27, 0x20000
	s_mov_b32 s26, 0x1080000
	s_and_b32 s25, s53, 0xffff
	s_mov_b32 s24, s52
	v_lshl_add_u64 v[100:101], s[58:59], 0, v[66:67]
	v_cmp_eq_u32_e64 s[18:19], 0, v0
	s_mul_i32 s29, s2, 0x5960
	s_movk_i32 s33, 0x7000
	v_add_u32_e32 v134, 0xffbe0000, v2
	v_mov_b32_e32 v108, v106
	v_mov_b32_e32 v109, v67
	s_movk_i32 s35, 0x1000
	s_movk_i32 s41, 0x2000
	s_movk_i32 s43, 0x3000
	s_movk_i32 s45, 0x5000
	s_movk_i32 s47, 0x6000
	s_mov_b32 s49, 0x8000
	s_mov_b32 s60, 0xa000
	s_mov_b32 s61, 0xb000
	s_mov_b32 s28, 0x3f3504f3
	s_mov_b32 s62, 0x378e98ab
	s_mov_b32 s63, 0x3b7cd369
	s_mov_b32 s64, 0xbcc618b2
	s_mov_b32 s65, 0x3dda74e4
	s_mov_b32 s66, 0x3f228afd
	s_mov_b32 s67, 0x3e03c728
	s_mov_b32 s68, 0xbfb8aa3b
	s_mov_b32 s69, 0x42ce8ed0
	s_mov_b32 s70, 0xc2b17218
	v_mov_b32_e32 v135, 0x3ba10414
	s_brev_b32 s71, -2
	s_mov_b32 s72, 0xf800000
	v_mov_b32_e32 v136, 0x260
	v_add_u32_e32 v137, v19, v20
	s_movk_i32 s73, 0x401
	s_mov_b32 s74, 0x3ea7ba05
	s_mov_b32 s34, 0xbfba00e3
	s_mov_b32 s40, 0x3f87dc22
	s_mov_b32 s42, 0x3fb5f0e3
	v_add_u32_e32 v138, v21, v22
	v_add_u32_e32 v139, v23, v24
	v_add_u32_e32 v140, v25, v26
	v_add_u32_e32 v141, v27, v12
	v_add_u32_e32 v142, v28, v14
	v_add_u32_e32 v143, v29, v16
	v_add_u32_e32 v144, v98, v6
	s_mov_b32 s75, 0x12000
	s_mov_b32 s76, 0x14000
	s_mov_b32 s77, 0x15000
	s_mov_b32 s78, 0x16000
	s_mov_b32 s79, 0x17000
	s_mov_b32 s80, 0x19000
	s_mov_b32 s81, 0x1a000
	s_mov_b32 s82, 0x1b000
	s_mov_b32 s83, 0x1c000
	s_mov_b32 s84, 0x1e000
	s_mov_b32 s85, 0x1f000
	s_mov_b32 s86, 0x21000
	s_mov_b32 s87, 0x23000
	s_mov_b32 s88, 0x24000
	s_mov_b32 s89, 0x25000
	s_mov_b32 s90, 0x26000
	s_mov_b32 s91, 0x28000
	s_mov_b32 s92, 0x29000
	s_mov_b32 s93, 0x2a000
	v_mov_b32_e32 v145, 1
	v_mov_b32_e32 v146, 0xb9c68948
	v_mov_b32_e32 v147, 0x7f800000
	v_mov_b32_e32 v148, v67
	v_mov_b32_e32 v149, v67
	v_mov_b32_e32 v150, v67
	v_mov_b32_e32 v151, v67
	s_mov_b32 s44, 0xbe91a98e
	s_mov_b32 s46, 0x3e827906
	s_mov_b32 s48, 0x4038aa3b
	s_mov_b64 s[98:99], exec
	s_and_b64 exec, s[98:99], s[4:5]
	global_load_dword v244, v[70:71], off
	global_load_dword v245, v[72:73], off
	global_load_dword v246, v[72:73], off offset:64
	s_and_b64 exec, s[98:99], s[22:23]
	global_load_dword v247, v[76:77], off
	global_load_dword v248, v[74:75], off
	s_and_b64 exec, s[98:99], s[6:7]
	global_load_dword v249, v[80:81], off
	global_load_dword v250, v[78:79], off
	global_load_dword v251, v[82:83], off
	global_load_dword v252, v[84:85], off
	global_load_dword v253, v[86:87], off
	s_mov_b64 exec, s[98:99]
	v_mov_b32_e32 v254, 0x1000
	v_mov_b32_e32 v255, 0
	v_lshl_add_u64 v[254:255], v[100:101], 0, v[254:255]
	global_load_dword v244, v[100:101], off
	global_load_dword v245, v[100:101], off offset:1024
	global_load_dword v246, v[100:101], off offset:2048
	global_load_dword v247, v[100:101], off offset:3072
	global_load_dword v248, v[254:255], off
	global_load_dword v249, v[254:255], off offset:1024
	global_load_dword v250, v[254:255], off offset:2048
	global_load_dword v251, v[254:255], off offset:3072
	global_load_dword v252, v[102:103], off
	global_load_dword v253, v[102:103], off offset:64
	global_load_dword v244, v[102:103], off offset:128
	global_load_dword v245, v[102:103], off offset:192
	s_branch .LBB3_4

	.amdhsa_kernel _Z10k_enc_scanPKDF16_PKfS2_S2_S2_S2_S2_S2_S2_S2_S2_S0_S2_S2_S2_S2_S2_S0_S2_PfPjS2_S2_S2_S2_S2_S2_S2_S2_S2_S2_S2_S2_PDF16_S5_S3_
		.amdhsa_group_segment_fixed_size 91136
		.amdhsa_private_segment_fixed_size 0
		.amdhsa_kernarg_size 288
		.amdhsa_user_sgpr_count 2
		.amdhsa_user_sgpr_dispatch_ptr 0
		.amdhsa_user_sgpr_queue_ptr 0
		.amdhsa_user_sgpr_kernarg_segment_ptr 1
		.amdhsa_user_sgpr_dispatch_id 0
		.amdhsa_user_sgpr_kernarg_preload_length 0
		.amdhsa_user_sgpr_kernarg_preload_offset 0
		.amdhsa_user_sgpr_private_segment_size 0
		.amdhsa_uses_dynamic_stack 0
		.amdhsa_enable_private_segment 0
		.amdhsa_system_sgpr_workgroup_id_x 1
		.amdhsa_system_sgpr_workgroup_id_y 0
		.amdhsa_system_sgpr_workgroup_id_z 0
		.amdhsa_system_sgpr_workgroup_info 0
		.amdhsa_system_vgpr_workitem_id 0
		.amdhsa_next_free_vgpr 256
		.amdhsa_next_free_sgpr 100
		.amdhsa_accum_offset 256
		.amdhsa_reserve_vcc 1
		.amdhsa_float_round_mode_32 0
		.amdhsa_float_round_mode_16_64 0
		.amdhsa_float_denorm_mode_32 3
		.amdhsa_float_denorm_mode_16_64 3
		.amdhsa_dx10_clamp 1
		.amdhsa_ieee_mode 1
		.amdhsa_fp16_overflow 0
		.amdhsa_tg_split 0
		.amdhsa_exception_fp_ieee_invalid_op 0
		.amdhsa_exception_fp_denorm_src 0
		.amdhsa_exception_fp_ieee_div_zero 0
		.amdhsa_exception_fp_ieee_overflow 0
		.amdhsa_exception_fp_ieee_underflow 0
		.amdhsa_exception_fp_ieee_inexact 0
		.amdhsa_exception_int_div_zero 0
	.end_amdhsa_kernel

amdhsa.kernels:
  - .agpr_count:     8
    .args:
      - .actual_access:  read_only
        .address_space:  global
        .offset:         0
        .size:           8
        .value_kind:     global_buffer
      - .actual_access:  read_only
        .address_space:  global
        .offset:         8
        .size:           8
        .value_kind:     global_buffer
      - .actual_access:  write_only
        .address_space:  global
        .offset:         16
        .size:           8
        .value_kind:     global_buffer
      - .actual_access:  write_only
        .address_space:  global
        .offset:         24
        .size:           8
        .value_kind:     global_buffer
      - .actual_access:  read_only
        .address_space:  global
        .offset:         32
        .size:           8
        .value_kind:     global_buffer
      - .actual_access:  read_only
        .address_space:  global
        .offset:         40
        .size:           8
        .value_kind:     global_buffer
      - .actual_access:  write_only
        .address_space:  global
        .offset:         48
        .size:           8
        .value_kind:     global_buffer
      - .actual_access:  write_only
        .address_space:  global
        .offset:         56
        .size:           8
        .value_kind:     global_buffer
      - .actual_access:  write_only
        .address_space:  global
        .offset:         64
        .size:           8
        .value_kind:     global_buffer
    .group_segment_fixed_size: 24976
    .kernarg_segment_align: 8
    .kernarg_segment_size: 72
    .language:       OpenCL C
    .language_version:
      - 2
      - 0
    .max_flat_workgroup_size: 256
    .name:           _Z9k_fb_mfmaPKfS0_PDF16_PfS0_S0_S1_S1_Pj
    .private_segment_fixed_size: 0
    .sgpr_count:     24
    .sgpr_spill_count: 0
    .symbol:         _Z9k_fb_mfmaPKfS0_PDF16_PfS0_S0_S1_S1_Pj.kd
    .uniform_work_group_size: 1
    .uses_dynamic_stack: false
    .vgpr_count:     92
    .vgpr_spill_count: 0
    .wavefront_size: 64
  - .agpr_count:     0
    .args:
      - .actual_access:  read_only
        .address_space:  global
        .offset:         0
        .size:           8
        .value_kind:     global_buffer
      - .actual_access:  read_only
        .address_space:  global
        .offset:         8
        .size:           8
        .value_kind:     global_buffer
      - .actual_access:  write_only
        .address_space:  global
        .offset:         16
        .size:           8
        .value_kind:     global_buffer
      - .actual_access:  write_only
        .address_space:  global
        .offset:         24
        .size:           8
        .value_kind:     global_buffer
    .group_segment_fixed_size: 0
    .kernarg_segment_align: 8
    .kernarg_segment_size: 32
    .language:       OpenCL C
    .language_version:
      - 2
      - 0
    .max_flat_workgroup_size: 1024
    .name:           _Z6k_prepPKfS0_PDF16_S1_
    .private_segment_fixed_size: 0
    .sgpr_count:     19
    .sgpr_spill_count: 0
    .symbol:         _Z6k_prepPKfS0_PDF16_S1_.kd
    .uniform_work_group_size: 1
    .uses_dynamic_stack: false
    .vgpr_count:     8
    .vgpr_spill_count: 0
    .wavefront_size: 64
  - .agpr_count:     0
    .args:
      - .actual_access:  read_only
        .address_space:  global
        .offset:         0
        .size:           8
        .value_kind:     global_buffer
      - .actual_access:  read_only
        .address_space:  global
        .offset:         8
        .size:           8
        .value_kind:     global_buffer
      - .actual_access:  read_only
        .address_space:  global
        .offset:         16
        .size:           8
        .value_kind:     global_buffer
      - .actual_access:  read_only
        .address_space:  global
        .offset:         24
        .size:           8
        .value_kind:     global_buffer
      - .actual_access:  read_only
        .address_space:  global
        .offset:         32
        .size:           8
        .value_kind:     global_buffer
      - .actual_access:  read_only
        .address_space:  global
        .offset:         40
        .size:           8
        .value_kind:     global_buffer
      - .actual_access:  read_only
        .address_space:  global
        .offset:         48
        .size:           8
        .value_kind:     global_buffer
      - .actual_access:  read_only
        .address_space:  global
        .offset:         56
        .size:           8
        .value_kind:     global_buffer
      - .actual_access:  read_only
        .address_space:  global
        .offset:         64
        .size:           8
        .value_kind:     global_buffer
      - .actual_access:  read_only
        .address_space:  global
        .offset:         72
        .size:           8
        .value_kind:     global_buffer
      - .actual_access:  write_only
        .address_space:  global
        .offset:         80
        .size:           8
        .value_kind:     global_buffer
      - .actual_access:  write_only
        .address_space:  global
        .offset:         88
        .size:           8
        .value_kind:     global_buffer
    .group_segment_fixed_size: 236
    .kernarg_segment_align: 8
    .kernarg_segment_size: 96
    .language:       OpenCL C
    .language_version:
      - 2
      - 0
    .max_flat_workgroup_size: 192
    .name:           _Z6k_gatePKfS0_S0_S0_S0_S0_S0_S0_S0_S0_PfPj
    .private_segment_fixed_size: 0
    .sgpr_count:     32
    .sgpr_spill_count: 0
    .symbol:         _Z6k_gatePKfS0_S0_S0_S0_S0_S0_S0_S0_S0_PfPj.kd
    .uniform_work_group_size: 1
    .uses_dynamic_stack: false
    .vgpr_count:     47
    .vgpr_spill_count: 0
    .wavefront_size: 64
  - .agpr_count:     0
    .args:
      - .actual_access:  read_only
        .address_space:  global
        .offset:         0
        .size:           8
        .value_kind:     global_buffer
      - .actual_access:  read_only
        .address_space:  global
        .offset:         8
        .size:           8
        .value_kind:     global_buffer
      - .actual_access:  read_only
        .address_space:  global
        .offset:         16
        .size:           8
        .value_kind:     global_buffer
      - .actual_access:  read_only
        .address_space:  global
        .offset:         24
        .size:           8
        .value_kind:     global_buffer
      - .actual_access:  read_only
        .address_space:  global
        .offset:         32
        .size:           8
        .value_kind:     global_buffer
      - .actual_access:  read_only
        .address_space:  global
        .offset:         40
        .size:           8
        .value_kind:     global_buffer
      - .actual_access:  read_only
        .address_space:  global
        .offset:         48
        .size:           8
        .value_kind:     global_buffer
      - .actual_access:  read_only
        .address_space:  global
        .offset:         56
        .size:           8
        .value_kind:     global_buffer
      - .actual_access:  read_only
        .address_space:  global
        .offset:         64
        .size:           8
        .value_kind:     global_buffer
      - .actual_access:  read_only
        .address_space:  global
        .offset:         72
        .size:           8
        .value_kind:     global_buffer
      - .actual_access:  read_only
        .address_space:  global
        .offset:         80
        .size:           8
        .value_kind:     global_buffer
      - .actual_access:  read_only
        .address_space:  global
        .offset:         88
        .size:           8
        .value_kind:     global_buffer
      - .actual_access:  read_only
        .address_space:  global
        .offset:         96
        .size:           8
        .value_kind:     global_buffer
      - .actual_access:  read_only
        .address_space:  global
        .offset:         104
        .size:           8
        .value_kind:     global_buffer
      - .actual_access:  read_only
        .address_space:  global
        .offset:         112
        .size:           8
        .value_kind:     global_buffer
      - .actual_access:  read_only
        .address_space:  global
        .offset:         120
        .size:           8
        .value_kind:     global_buffer
      - .actual_access:  read_only
        .address_space:  global
        .offset:         128
        .size:           8
        .value_kind:     global_buffer
      - .actual_access:  read_only
        .address_space:  global
        .offset:         136
        .size:           8
        .value_kind:     global_buffer
      - .actual_access:  read_only
        .address_space:  global
        .offset:         144
        .size:           8
        .value_kind:     global_buffer
      - .address_space:  global
        .offset:         152
        .size:           8
        .value_kind:     global_buffer
      - .address_space:  global
        .offset:         160
        .size:           8
        .value_kind:     global_buffer
      - .actual_access:  read_only
        .address_space:  global
        .offset:         168
        .size:           8
        .value_kind:     global_buffer
      - .actual_access:  read_only
        .address_space:  global
        .offset:         176
        .size:           8
        .value_kind:     global_buffer
      - .actual_access:  read_only
        .address_space:  global
        .offset:         184
        .size:           8
        .value_kind:     global_buffer
      - .actual_access:  read_only
        .address_space:  global
        .offset:         192
        .size:           8
        .value_kind:     global_buffer
      - .actual_access:  read_only
        .address_space:  global
        .offset:         200
        .size:           8
        .value_kind:     global_buffer
      - .actual_access:  read_only
        .address_space:  global
        .offset:         208
        .size:           8
        .value_kind:     global_buffer
      - .actual_access:  read_only
        .address_space:  global
        .offset:         216
        .size:           8
        .value_kind:     global_buffer
      - .actual_access:  read_only
        .address_space:  global
        .offset:         224
        .size:           8
        .value_kind:     global_buffer
      - .actual_access:  read_only
        .address_space:  global
        .offset:         232
        .size:           8
        .value_kind:     global_buffer
      - .actual_access:  read_only
        .address_space:  global
        .offset:         240
        .size:           8
        .value_kind:     global_buffer
      - .actual_access:  read_only
        .address_space:  global
        .offset:         248
        .size:           8
        .value_kind:     global_buffer
      - .actual_access:  read_only
        .address_space:  global
        .offset:         256
        .size:           8
        .value_kind:     global_buffer
      - .actual_access:  write_only
        .address_space:  global
        .offset:         264
        .size:           8
        .value_kind:     global_buffer
      - .actual_access:  write_only
        .address_space:  global
        .offset:         272
        .size:           8
        .value_kind:     global_buffer
      - .actual_access:  write_only
        .address_space:  global
        .offset:         280
        .size:           8
        .value_kind:     global_buffer
    .group_segment_fixed_size: 91136
    .kernarg_segment_align: 8
    .kernarg_segment_size: 288
    .language:       OpenCL C
    .language_version:
      - 2
      - 0
    .max_flat_workgroup_size: 320
    .name:           _Z10k_enc_scanPKDF16_PKfS2_S2_S2_S2_S2_S2_S2_S2_S2_S0_S2_S2_S2_S2_S2_S0_S2_PfPjS2_S2_S2_S2_S2_S2_S2_S2_S2_S2_S2_S2_PDF16_S5_S3_
    .private_segment_fixed_size: 0
    .sgpr_count:     106
    .sgpr_spill_count: 0
    .symbol:         _Z10k_enc_scanPKDF16_PKfS2_S2_S2_S2_S2_S2_S2_S2_S2_S0_S2_S2_S2_S2_S2_S0_S2_PfPjS2_S2_S2_S2_S2_S2_S2_S2_S2_S2_S2_S2_PDF16_S5_S3_.kd
    .uniform_work_group_size: 1
    .uses_dynamic_stack: false
    .vgpr_count:     256
    .vgpr_spill_count: 0
    .wavefront_size: 64
  - .agpr_count:     0
    .args:
      - .actual_access:  read_only
        .address_space:  global
        .offset:         0
        .size:           8
        .value_kind:     global_buffer
      - .actual_access:  read_only
        .address_space:  global
        .offset:         8
        .size:           8
        .value_kind:     global_buffer
      - .actual_access:  write_only
        .address_space:  global
        .offset:         16
        .size:           8
        .value_kind:     global_buffer
    .group_segment_fixed_size: 66580
    .kernarg_segment_align: 8
    .kernarg_segment_size: 24
    .language:       OpenCL C
    .language_version:
      - 2
      - 0
    .max_flat_workgroup_size: 320
    .name:           _Z7k_att1nPKDF16_S0_Pf
    .private_segment_fixed_size: 0
    .sgpr_count:     29
    .sgpr_spill_count: 0
    .symbol:         _Z7k_att1nPKDF16_S0_Pf.kd
    .uniform_work_group_size: 1
    .uses_dynamic_stack: false
    .vgpr_count:     126
    .vgpr_spill_count: 0
    .wavefront_size: 64
  - .agpr_count:     0
    .args:
      - .actual_access:  read_only
        .address_space:  global
        .offset:         0
        .size:           8
        .value_kind:     global_buffer
      - .actual_access:  read_only
        .address_space:  global
        .offset:         8
        .size:           8
        .value_kind:     global_buffer
      - .actual_access:  read_only
        .address_space:  global
        .offset:         16
        .size:           8
        .value_kind:     global_buffer
      - .actual_access:  write_only
        .address_space:  global
        .offset:         24
        .size:           8
        .value_kind:     global_buffer
      - .actual_access:  read_only
        .address_space:  global
        .offset:         32
        .size:           8
        .value_kind:     global_buffer
      - .actual_access:  read_only
        .address_space:  global
        .offset:         40
        .size:           8
        .value_kind:     global_buffer
      - .actual_access:  read_only
        .address_space:  global
        .offset:         48
        .size:           8
        .value_kind:     global_buffer
      - .actual_access:  read_only
        .address_space:  global
        .offset:         56
        .size:           8
        .value_kind:     global_buffer
      - .actual_access:  read_only
        .address_space:  global
        .offset:         64
        .size:           8
        .value_kind:     global_buffer
      - .actual_access:  read_only
        .address_space:  global
        .offset:         72
        .size:           8
        .value_kind:     global_buffer
      - .actual_access:  read_only
        .address_space:  global
        .offset:         80
        .size:           8
        .value_kind:     global_buffer
      - .actual_access:  read_only
        .address_space:  global
        .offset:         88
        .size:           8
        .value_kind:     global_buffer
      - .actual_access:  read_only
        .address_space:  global
        .offset:         96
        .size:           8
        .value_kind:     global_buffer
      - .actual_access:  write_only
        .address_space:  global
        .offset:         104
        .size:           8
        .value_kind:     global_buffer
    .group_segment_fixed_size: 70720
    .kernarg_segment_align: 8
    .kernarg_segment_size: 112
    .language:       OpenCL C
    .language_version:
      - 2
      - 0
    .max_flat_workgroup_size: 320
    .name:           _Z7k_att2nPKDF16_S0_PKfPfS2_S2_S2_S2_S2_S2_S2_S2_S2_S3_
    .private_segment_fixed_size: 0
    .sgpr_count:     58
    .sgpr_spill_count: 0
    .symbol:         _Z7k_att2nPKDF16_S0_PKfPfS2_S2_S2_S2_S2_S2_S2_S2_S2_S3_.kd
    .uniform_work_group_size: 1
    .uses_dynamic_stack: false
    .vgpr_count:     122
    .vgpr_spill_count: 0
    .wavefront_size: 64
  - .agpr_count:     0
    .args:
      - .actual_access:  read_only
        .address_space:  global
        .offset:         0
        .size:           8
        .value_kind:     global_buffer
      - .actual_access:  read_only
        .address_space:  global
        .offset:         8
        .size:           8
        .value_kind:     global_buffer
      - .actual_access:  read_only
        .address_space:  global
        .offset:         16
        .size:           8
        .value_kind:     global_buffer
      - .actual_access:  read_only
        .address_space:  global
        .offset:         24
        .size:           8
        .value_kind:     global_buffer
      - .actual_access:  read_only
        .address_space:  global
        .offset:         32
        .size:           8
        .value_kind:     global_buffer
      - .actual_access:  read_only
        .address_space:  global
        .offset:         40
        .size:           8
        .value_kind:     global_buffer
      - .actual_access:  read_only
        .address_space:  global
        .offset:         48
        .size:           8
        .value_kind:     global_buffer
      - .actual_access:  read_only
        .address_space:  global
        .offset:         56
        .size:           8
        .value_kind:     global_buffer
      - .actual_access:  read_only
        .address_space:  global
        .offset:         64
        .size:           8
        .value_kind:     global_buffer
      - .actual_access:  write_only
        .address_space:  global
        .offset:         72
        .size:           8
        .value_kind:     global_buffer
    .group_segment_fixed_size: 704
    .kernarg_segment_align: 8
    .kernarg_segment_size: 80
    .language:       OpenCL C
    .language_version:
      - 2
      - 0
    .max_flat_workgroup_size: 64
    .name:           _Z8k_heads3PKfS0_S0_S0_S0_S0_S0_S0_S0_Pf
    .private_segment_fixed_size: 0
    .sgpr_count:     24
    .sgpr_spill_count: 0
    .symbol:         _Z8k_heads3PKfS0_S0_S0_S0_S0_S0_S0_S0_Pf.kd
    .uniform_work_group_size: 1
    .uses_dynamic_stack: false
    .vgpr_count:     121
    .vgpr_spill_count: 0
    .wavefront_size: 64
